# all per-phase s_setprio flips removed from the four GEMM K-loops (on v40)
# baseline (speedup 1.0000x reference)
.LBB3_34:
	s_mov_b32 m0, s66
	ds_read_b128 v[98:101], v94 offset:16384
	ds_read_b128 v[102:105], v94 offset:17408
	ds_read_b128 v[106:109], v94 offset:18432
	ds_read_b128 v[110:113], v94 offset:19456
	ds_read_b128 v[114:117], v95
	ds_read_b128 v[118:121], v95 offset:1024
	ds_read_b128 v[122:125], v95 offset:2048
	ds_read_b128 v[126:129], v95 offset:3072
	ds_read_b128 v[130:133], v95 offset:4096
	ds_read_b128 v[134:137], v95 offset:5120
	ds_read_b128 v[138:141], v95 offset:6144
	ds_read_b128 v[142:145], v95 offset:7168
	global_load_lds_dwordx4 v60, s[68:69]
	s_add_i32 m0, s66, 0x2000
	s_nop 0
	global_load_lds_dwordx4 v62, s[68:69]
	s_barrier
	s_waitcnt lgkmcnt(7)
	v_mfma_f32_16x16x32_f16 v[44:47], v[98:101], v[114:117], v[44:47]
	v_mfma_f32_16x16x32_f16 v[40:43], v[106:109], v[114:117], v[40:43]
	s_waitcnt lgkmcnt(5)
	v_mfma_f32_16x16x32_f16 v[32:35], v[98:101], v[122:125], v[32:35]
	v_mfma_f32_16x16x32_f16 v[28:31], v[106:109], v[122:125], v[28:31]
	s_waitcnt lgkmcnt(3)
	v_mfma_f32_16x16x32_f16 v[20:23], v[98:101], v[130:133], v[20:23]
	v_mfma_f32_16x16x32_f16 v[16:19], v[106:109], v[130:133], v[16:19]
	s_waitcnt lgkmcnt(1)
	v_mfma_f32_16x16x32_f16 v[8:11], v[98:101], v[138:141], v[8:11]
	v_mfma_f32_16x16x32_f16 v[4:7], v[106:109], v[138:141], v[4:7]
	v_mfma_f32_16x16x32_f16 v[44:47], v[102:105], v[118:121], v[44:47]
	v_mfma_f32_16x16x32_f16 v[40:43], v[110:113], v[118:121], v[40:43]
	v_mfma_f32_16x16x32_f16 v[32:35], v[102:105], v[126:129], v[32:35]
	v_mfma_f32_16x16x32_f16 v[28:31], v[110:113], v[126:129], v[28:31]
	v_mfma_f32_16x16x32_f16 v[20:23], v[102:105], v[134:137], v[20:23]
	v_mfma_f32_16x16x32_f16 v[16:19], v[110:113], v[134:137], v[16:19]
	s_waitcnt lgkmcnt(0)
	v_mfma_f32_16x16x32_f16 v[8:11], v[102:105], v[142:145], v[8:11]
	v_mfma_f32_16x16x32_f16 v[4:7], v[110:113], v[142:145], v[4:7]
	s_barrier
	s_add_i32 m0, s43, 0x18000
	ds_read_b128 v[98:101], v94 offset:20480
	ds_read_b128 v[102:105], v94 offset:21504
	global_load_lds_dwordx4 v64, s[70:71]
	s_add_i32 m0, s43, 0x1a000
	s_nop 0
	global_load_lds_dwordx4 v66, s[70:71]
	s_add_i32 m0, s43, 0x1c000
	s_nop 0
	global_load_lds_dwordx4 v68, s[70:71]
	s_waitcnt vmcnt(5)
	s_barrier
	s_waitcnt lgkmcnt(1)
	v_mfma_f32_16x16x32_f16 v[36:39], v[98:101], v[114:117], v[36:39]
	v_mfma_f32_16x16x32_f16 v[24:27], v[98:101], v[122:125], v[24:27]
	v_mfma_f32_16x16x32_f16 v[12:15], v[98:101], v[130:133], v[12:15]
	v_mfma_f32_16x16x32_f16 v[0:3], v[98:101], v[138:141], v[0:3]
	s_waitcnt lgkmcnt(0)
	v_mfma_f32_16x16x32_f16 v[36:39], v[102:105], v[118:121], v[36:39]
	v_mfma_f32_16x16x32_f16 v[24:27], v[102:105], v[126:129], v[24:27]
	v_mfma_f32_16x16x32_f16 v[12:15], v[102:105], v[134:137], v[12:15]
	v_mfma_f32_16x16x32_f16 v[0:3], v[102:105], v[142:145], v[0:3]
	s_barrier
	s_mov_b32 m0, s43
	ds_read_b128 v[98:101], v94 offset:57344
	ds_read_b128 v[102:105], v94 offset:58368
	ds_read_b128 v[106:109], v94 offset:59392
	ds_read_b128 v[110:113], v94 offset:60416
	ds_read_b128 v[114:117], v95 offset:40960
	ds_read_b128 v[118:121], v95 offset:41984
	ds_read_b128 v[122:125], v95 offset:43008
	ds_read_b128 v[126:129], v95 offset:44032
	ds_read_b128 v[130:133], v95 offset:45056
	ds_read_b128 v[134:137], v95 offset:46080
	ds_read_b128 v[138:141], v95 offset:47104
	ds_read_b128 v[142:145], v95 offset:48128
	global_load_lds_dwordx4 v48, s[64:65]
	s_mov_b32 m0, s44
	s_nop 0
	global_load_lds_dwordx4 v52, s[64:65]
	s_barrier
	s_waitcnt lgkmcnt(7)
	v_mfma_f32_16x16x32_f16 v[44:47], v[98:101], v[114:117], v[44:47]
	v_mfma_f32_16x16x32_f16 v[40:43], v[106:109], v[114:117], v[40:43]
	s_waitcnt lgkmcnt(5)
	v_mfma_f32_16x16x32_f16 v[32:35], v[98:101], v[122:125], v[32:35]
	v_mfma_f32_16x16x32_f16 v[28:31], v[106:109], v[122:125], v[28:31]
	s_waitcnt lgkmcnt(3)
	v_mfma_f32_16x16x32_f16 v[20:23], v[98:101], v[130:133], v[20:23]
	v_mfma_f32_16x16x32_f16 v[16:19], v[106:109], v[130:133], v[16:19]
	s_waitcnt lgkmcnt(1)
	v_mfma_f32_16x16x32_f16 v[8:11], v[98:101], v[138:141], v[8:11]
	v_mfma_f32_16x16x32_f16 v[4:7], v[106:109], v[138:141], v[4:7]
	v_mfma_f32_16x16x32_f16 v[44:47], v[102:105], v[118:121], v[44:47]
	v_mfma_f32_16x16x32_f16 v[40:43], v[110:113], v[118:121], v[40:43]
	v_mfma_f32_16x16x32_f16 v[32:35], v[102:105], v[126:129], v[32:35]
	v_mfma_f32_16x16x32_f16 v[28:31], v[110:113], v[126:129], v[28:31]
	v_mfma_f32_16x16x32_f16 v[20:23], v[102:105], v[134:137], v[20:23]
	v_mfma_f32_16x16x32_f16 v[16:19], v[110:113], v[134:137], v[16:19]
	s_waitcnt lgkmcnt(0)
	v_mfma_f32_16x16x32_f16 v[8:11], v[102:105], v[142:145], v[8:11]
	v_mfma_f32_16x16x32_f16 v[4:7], v[110:113], v[142:145], v[4:7]
	s_barrier
	s_mov_b32 m0, s45
	ds_read_b128 v[98:101], v94 offset:61440
	ds_read_b128 v[102:105], v94 offset:62464
	global_load_lds_dwordx4 v50, s[26:27]
	s_mov_b32 m0, s46
	s_nop 0
	global_load_lds_dwordx4 v54, s[26:27]
	s_mov_b32 m0, s47
	s_nop 0
	global_load_lds_dwordx4 v56, s[26:27]
	s_waitcnt vmcnt(5)
	s_barrier
	s_waitcnt lgkmcnt(1)
	v_mfma_f32_16x16x32_f16 v[36:39], v[98:101], v[114:117], v[36:39]
	v_mfma_f32_16x16x32_f16 v[24:27], v[98:101], v[122:125], v[24:27]
	v_mfma_f32_16x16x32_f16 v[12:15], v[98:101], v[130:133], v[12:15]
	v_mfma_f32_16x16x32_f16 v[0:3], v[98:101], v[138:141], v[0:3]
	s_waitcnt lgkmcnt(0)
	v_mfma_f32_16x16x32_f16 v[36:39], v[102:105], v[118:121], v[36:39]
	v_mfma_f32_16x16x32_f16 v[24:27], v[102:105], v[126:129], v[24:27]
	v_mfma_f32_16x16x32_f16 v[12:15], v[102:105], v[134:137], v[12:15]
	v_mfma_f32_16x16x32_f16 v[0:3], v[102:105], v[142:145], v[0:3]
	s_barrier
	s_mov_b32 m0, s52
	ds_read_b128 v[98:101], v96
	ds_read_b128 v[102:105], v96 offset:1024
	ds_read_b128 v[106:109], v96 offset:2048
	ds_read_b128 v[110:113], v96 offset:3072
	ds_read_b128 v[114:117], v97
	ds_read_b128 v[118:121], v97 offset:1024
	ds_read_b128 v[122:125], v97 offset:2048
	ds_read_b128 v[126:129], v97 offset:3072
	ds_read_b128 v[130:133], v97 offset:4096
	ds_read_b128 v[134:137], v97 offset:5120
	ds_read_b128 v[138:141], v97 offset:6144
	ds_read_b128 v[142:145], v97 offset:7168
	global_load_lds_dwordx4 v48, s[72:73]
	s_mov_b32 m0, s53
	s_nop 0
	global_load_lds_dwordx4 v52, s[72:73]
	s_barrier
	s_waitcnt lgkmcnt(7)
	v_mfma_f32_16x16x32_f16 v[44:47], v[98:101], v[114:117], v[44:47]
	v_mfma_f32_16x16x32_f16 v[40:43], v[106:109], v[114:117], v[40:43]
	s_waitcnt lgkmcnt(5)
	v_mfma_f32_16x16x32_f16 v[32:35], v[98:101], v[122:125], v[32:35]
	v_mfma_f32_16x16x32_f16 v[28:31], v[106:109], v[122:125], v[28:31]
	s_waitcnt lgkmcnt(3)
	v_mfma_f32_16x16x32_f16 v[20:23], v[98:101], v[130:133], v[20:23]
	v_mfma_f32_16x16x32_f16 v[16:19], v[106:109], v[130:133], v[16:19]
	s_waitcnt lgkmcnt(1)
	v_mfma_f32_16x16x32_f16 v[8:11], v[98:101], v[138:141], v[8:11]
	v_mfma_f32_16x16x32_f16 v[4:7], v[106:109], v[138:141], v[4:7]
	v_mfma_f32_16x16x32_f16 v[44:47], v[102:105], v[118:121], v[44:47]
	v_mfma_f32_16x16x32_f16 v[40:43], v[110:113], v[118:121], v[40:43]
	v_mfma_f32_16x16x32_f16 v[32:35], v[102:105], v[126:129], v[32:35]
	v_mfma_f32_16x16x32_f16 v[28:31], v[110:113], v[126:129], v[28:31]
	v_mfma_f32_16x16x32_f16 v[20:23], v[102:105], v[134:137], v[20:23]
	v_mfma_f32_16x16x32_f16 v[16:19], v[110:113], v[134:137], v[16:19]
	s_waitcnt lgkmcnt(0)
	v_mfma_f32_16x16x32_f16 v[8:11], v[102:105], v[142:145], v[8:11]
	v_mfma_f32_16x16x32_f16 v[4:7], v[110:113], v[142:145], v[4:7]
	s_barrier
	s_mov_b32 m0, s54
	ds_read_b128 v[98:101], v96 offset:4096
	ds_read_b128 v[102:105], v96 offset:5120
	global_load_lds_dwordx4 v50, s[74:75]
	s_add_i32 m0, s54, 0x2000
	s_nop 0
	global_load_lds_dwordx4 v54, s[74:75]
	s_add_i32 m0, s54, 0x4000
	s_nop 0
	global_load_lds_dwordx4 v56, s[74:75]
	s_waitcnt vmcnt(5)
	s_barrier
	s_waitcnt lgkmcnt(1)
	v_mfma_f32_16x16x32_f16 v[36:39], v[98:101], v[114:117], v[36:39]
	v_mfma_f32_16x16x32_f16 v[24:27], v[98:101], v[122:125], v[24:27]
	v_mfma_f32_16x16x32_f16 v[12:15], v[98:101], v[130:133], v[12:15]
	v_mfma_f32_16x16x32_f16 v[0:3], v[98:101], v[138:141], v[0:3]
	s_waitcnt lgkmcnt(0)
	v_mfma_f32_16x16x32_f16 v[36:39], v[102:105], v[118:121], v[36:39]
	v_mfma_f32_16x16x32_f16 v[24:27], v[102:105], v[126:129], v[24:27]
	v_mfma_f32_16x16x32_f16 v[12:15], v[102:105], v[134:137], v[12:15]
	v_mfma_f32_16x16x32_f16 v[0:3], v[102:105], v[142:145], v[0:3]
	s_add_i32 s63, s63, 3
	s_add_u32 s24, s24, 0x180
	s_addc_u32 s25, s25, 0
	s_cmp_ge_i32 s63, s49
	s_cbranch_scc1 .Lrot_exit_qkv
	s_add_u32 s68, s20, s24
	s_addc_u32 s69, s21, s25
	s_add_u32 s70, s22, s24
	s_addc_u32 s71, s23, s25
	s_add_u32 s26, s20, s24
	s_addc_u32 s27, s21, s25
	s_add_u32 s26, s26, 0x180
	s_addc_u32 s27, s27, 0
	s_add_u32 s64, s22, s24
	s_addc_u32 s65, s23, s25
	s_add_u32 s66, s64, 0x180
	s_addc_u32 s67, s65, 0
	s_cmp_eq_u32 s56, s63
	s_cselect_b32 s65, s5, s27
	s_cselect_b32 s64, s4, s26
	s_cselect_b32 s27, s7, s67
	s_cselect_b32 s26, s6, s66
	s_add_u32 s72, s64, 0x80
	s_addc_u32 s73, s65, 0
	s_add_u32 s74, s26, 0x80
	s_addc_u32 s75, s27, 0
	s_add_i32 s66, s58, s38
	s_barrier
	s_branch .LBB3_34

.LBB4_22:
	s_mov_b32 m0, s70
	ds_read_b128 v[130:133], v136 offset:16384
	ds_read_b128 v[142:145], v136 offset:17408
	ds_read_b128 v[146:149], v136 offset:18432
	ds_read_b128 v[150:153], v136 offset:19456
	ds_read_b128 v[154:157], v137
	ds_read_b128 v[158:161], v137 offset:1024
	ds_read_b128 v[162:165], v137 offset:2048
	ds_read_b128 v[166:169], v137 offset:3072
	ds_read_b128 v[170:173], v137 offset:4096
	ds_read_b128 v[174:177], v137 offset:5120
	ds_read_b128 v[178:181], v137 offset:6144
	ds_read_b128 v[182:185], v137 offset:7168
	global_load_lds_dwordx4 v0, s[74:75]
	s_add_i32 m0, s70, 0x2000
	s_nop 0
	global_load_lds_dwordx4 v120, s[74:75]
	s_barrier
	s_waitcnt lgkmcnt(7)
	v_mfma_f32_16x16x32_f16 v[94:97], v[130:133], v[154:157], v[94:97]
	v_mfma_f32_16x16x32_f16 v[90:93], v[146:149], v[154:157], v[90:93]
	s_waitcnt lgkmcnt(5)
	v_mfma_f32_16x16x32_f16 v[82:85], v[130:133], v[162:165], v[82:85]
	v_mfma_f32_16x16x32_f16 v[78:81], v[146:149], v[162:165], v[78:81]
	s_waitcnt lgkmcnt(3)
	v_mfma_f32_16x16x32_f16 v[70:73], v[130:133], v[170:173], v[70:73]
	v_mfma_f32_16x16x32_f16 v[66:69], v[146:149], v[170:173], v[66:69]
	s_waitcnt lgkmcnt(1)
	v_mfma_f32_16x16x32_f16 v[58:61], v[130:133], v[178:181], v[58:61]
	v_mfma_f32_16x16x32_f16 v[54:57], v[146:149], v[178:181], v[54:57]
	v_mfma_f32_16x16x32_f16 v[94:97], v[142:145], v[158:161], v[94:97]
	v_mfma_f32_16x16x32_f16 v[90:93], v[150:153], v[158:161], v[90:93]
	v_mfma_f32_16x16x32_f16 v[82:85], v[142:145], v[166:169], v[82:85]
	v_mfma_f32_16x16x32_f16 v[78:81], v[150:153], v[166:169], v[78:81]
	v_mfma_f32_16x16x32_f16 v[70:73], v[142:145], v[174:177], v[70:73]
	v_mfma_f32_16x16x32_f16 v[66:69], v[150:153], v[174:177], v[66:69]
	s_waitcnt lgkmcnt(0)
	v_mfma_f32_16x16x32_f16 v[58:61], v[142:145], v[182:185], v[58:61]
	v_mfma_f32_16x16x32_f16 v[54:57], v[150:153], v[182:185], v[54:57]
	s_barrier
	s_add_i32 m0, s49, 0x18000
	ds_read_b128 v[130:133], v136 offset:20480
	ds_read_b128 v[142:145], v136 offset:21504
	global_load_lds_dwordx4 v122, s[76:77]
	s_add_i32 m0, s49, 0x1a000
	s_nop 0
	global_load_lds_dwordx4 v124, s[76:77]
	s_add_i32 m0, s49, 0x1c000
	s_nop 0
	global_load_lds_dwordx4 v126, s[76:77]
	s_cmp_lg_u32 s67, 0
	s_cbranch_scc1 .Lpj_norm_0
	s_mul_i32 s72, s66, 0xc0
	v_add_u32_e32 v214, s72, v135
	v_ashrrev_i32_e32 v215, 31, v214
	v_lshl_add_u64 v[214:215], v[214:215], 2, s[10:11]
	global_load_dwordx4 v[202:205], v[214:215], off
	global_load_dwordx4 v[206:209], v[214:215], off offset:64
	global_load_dwordx4 v[210:213], v[214:215], off offset:128
	global_load_dwordx4 v[2:5], v[194:195], off
	global_load_dwordx4 v[6:9], v[194:195], off offset:64
	global_load_dwordx4 v[10:13], v[194:195], off offset:128
	global_load_dwordx4 v[14:17], v[196:197], off
	s_waitcnt vmcnt(12)
	s_branch .Lpj_join_0

.Lpj_join_0:
	s_barrier
	s_waitcnt lgkmcnt(1)
	v_mfma_f32_16x16x32_f16 v[86:89], v[130:133], v[154:157], v[86:89]
	v_mfma_f32_16x16x32_f16 v[74:77], v[130:133], v[162:165], v[74:77]
	v_mfma_f32_16x16x32_f16 v[62:65], v[130:133], v[170:173], v[62:65]
	v_mfma_f32_16x16x32_f16 v[50:53], v[130:133], v[178:181], v[50:53]
	s_waitcnt lgkmcnt(0)
	v_mfma_f32_16x16x32_f16 v[86:89], v[142:145], v[158:161], v[86:89]
	v_mfma_f32_16x16x32_f16 v[74:77], v[142:145], v[166:169], v[74:77]
	v_mfma_f32_16x16x32_f16 v[62:65], v[142:145], v[174:177], v[62:65]
	v_mfma_f32_16x16x32_f16 v[50:53], v[142:145], v[182:185], v[50:53]
	s_barrier
	s_mov_b32 m0, s49
	ds_read_b128 v[130:133], v136 offset:57344
	ds_read_b128 v[142:145], v136 offset:58368
	ds_read_b128 v[146:149], v136 offset:59392
	ds_read_b128 v[150:153], v136 offset:60416
	ds_read_b128 v[154:157], v137 offset:40960
	ds_read_b128 v[158:161], v137 offset:41984
	ds_read_b128 v[162:165], v137 offset:43008
	ds_read_b128 v[166:169], v137 offset:44032
	ds_read_b128 v[170:173], v137 offset:45056
	ds_read_b128 v[174:177], v137 offset:46080
	ds_read_b128 v[178:181], v137 offset:47104
	ds_read_b128 v[182:185], v137 offset:48128
	global_load_lds_dwordx4 v110, s[68:69]
	s_mov_b32 m0, s50
	s_nop 0
	global_load_lds_dwordx4 v114, s[68:69]
	s_barrier
	s_waitcnt lgkmcnt(7)
	v_mfma_f32_16x16x32_f16 v[94:97], v[130:133], v[154:157], v[94:97]
	v_mfma_f32_16x16x32_f16 v[90:93], v[146:149], v[154:157], v[90:93]
	s_waitcnt lgkmcnt(5)
	v_mfma_f32_16x16x32_f16 v[82:85], v[130:133], v[162:165], v[82:85]
	v_mfma_f32_16x16x32_f16 v[78:81], v[146:149], v[162:165], v[78:81]
	s_waitcnt lgkmcnt(3)
	v_mfma_f32_16x16x32_f16 v[70:73], v[130:133], v[170:173], v[70:73]
	v_mfma_f32_16x16x32_f16 v[66:69], v[146:149], v[170:173], v[66:69]
	s_waitcnt lgkmcnt(1)
	v_mfma_f32_16x16x32_f16 v[58:61], v[130:133], v[178:181], v[58:61]
	v_mfma_f32_16x16x32_f16 v[54:57], v[146:149], v[178:181], v[54:57]
	v_mfma_f32_16x16x32_f16 v[94:97], v[142:145], v[158:161], v[94:97]
	v_mfma_f32_16x16x32_f16 v[90:93], v[150:153], v[158:161], v[90:93]
	v_mfma_f32_16x16x32_f16 v[82:85], v[142:145], v[166:169], v[82:85]
	v_mfma_f32_16x16x32_f16 v[78:81], v[150:153], v[166:169], v[78:81]
	v_mfma_f32_16x16x32_f16 v[70:73], v[142:145], v[174:177], v[70:73]
	v_mfma_f32_16x16x32_f16 v[66:69], v[150:153], v[174:177], v[66:69]
	s_waitcnt lgkmcnt(0)
	v_mfma_f32_16x16x32_f16 v[58:61], v[142:145], v[182:185], v[58:61]
	v_mfma_f32_16x16x32_f16 v[54:57], v[150:153], v[182:185], v[54:57]
	s_barrier
	s_mov_b32 m0, s51
	ds_read_b128 v[130:133], v136 offset:61440
	ds_read_b128 v[142:145], v136 offset:62464
	global_load_lds_dwordx4 v112, s[34:35]
	s_mov_b32 m0, s52
	s_nop 0
	global_load_lds_dwordx4 v116, s[34:35]
	s_mov_b32 m0, s53
	s_nop 0
	global_load_lds_dwordx4 v118, s[34:35]
	s_cmp_lg_u32 s67, 0
	s_cbranch_scc1 .Lpj_norm_1
	global_load_dwordx4 v[18:21], v[196:197], off offset:64
	global_load_dwordx4 v[22:25], v[196:197], off offset:128
	global_load_dwordx4 v[26:29], v[198:199], off
	global_load_dwordx4 v[30:33], v[198:199], off offset:64
	s_waitcnt vmcnt(16)
	s_branch .Lpj_join_1

.Lpj_join_1:
	s_barrier
	s_waitcnt lgkmcnt(1)
	v_mfma_f32_16x16x32_f16 v[86:89], v[130:133], v[154:157], v[86:89]
	v_mfma_f32_16x16x32_f16 v[74:77], v[130:133], v[162:165], v[74:77]
	v_mfma_f32_16x16x32_f16 v[62:65], v[130:133], v[170:173], v[62:65]
	v_mfma_f32_16x16x32_f16 v[50:53], v[130:133], v[178:181], v[50:53]
	s_waitcnt lgkmcnt(0)
	v_mfma_f32_16x16x32_f16 v[86:89], v[142:145], v[158:161], v[86:89]
	v_mfma_f32_16x16x32_f16 v[74:77], v[142:145], v[166:169], v[74:77]
	v_mfma_f32_16x16x32_f16 v[62:65], v[142:145], v[174:177], v[62:65]
	v_mfma_f32_16x16x32_f16 v[50:53], v[142:145], v[182:185], v[50:53]
	s_barrier
	s_mov_b32 m0, s56
	ds_read_b128 v[130:133], v138
	ds_read_b128 v[142:145], v138 offset:1024
	ds_read_b128 v[146:149], v138 offset:2048
	ds_read_b128 v[150:153], v138 offset:3072
	ds_read_b128 v[154:157], v139
	ds_read_b128 v[158:161], v139 offset:1024
	ds_read_b128 v[162:165], v139 offset:2048
	ds_read_b128 v[166:169], v139 offset:3072
	ds_read_b128 v[170:173], v139 offset:4096
	ds_read_b128 v[174:177], v139 offset:5120
	ds_read_b128 v[178:181], v139 offset:6144
	ds_read_b128 v[182:185], v139 offset:7168
	global_load_lds_dwordx4 v110, s[78:79]
	s_mov_b32 m0, s57
	s_nop 0
	global_load_lds_dwordx4 v114, s[78:79]
	s_barrier
	s_waitcnt lgkmcnt(7)
	v_mfma_f32_16x16x32_f16 v[94:97], v[130:133], v[154:157], v[94:97]
	v_mfma_f32_16x16x32_f16 v[90:93], v[146:149], v[154:157], v[90:93]
	s_waitcnt lgkmcnt(5)
	v_mfma_f32_16x16x32_f16 v[82:85], v[130:133], v[162:165], v[82:85]
	v_mfma_f32_16x16x32_f16 v[78:81], v[146:149], v[162:165], v[78:81]
	s_waitcnt lgkmcnt(3)
	v_mfma_f32_16x16x32_f16 v[70:73], v[130:133], v[170:173], v[70:73]
	v_mfma_f32_16x16x32_f16 v[66:69], v[146:149], v[170:173], v[66:69]
	s_waitcnt lgkmcnt(1)
	v_mfma_f32_16x16x32_f16 v[58:61], v[130:133], v[178:181], v[58:61]
	v_mfma_f32_16x16x32_f16 v[54:57], v[146:149], v[178:181], v[54:57]
	v_mfma_f32_16x16x32_f16 v[94:97], v[142:145], v[158:161], v[94:97]
	v_mfma_f32_16x16x32_f16 v[90:93], v[150:153], v[158:161], v[90:93]
	v_mfma_f32_16x16x32_f16 v[82:85], v[142:145], v[166:169], v[82:85]
	v_mfma_f32_16x16x32_f16 v[78:81], v[150:153], v[166:169], v[78:81]
	v_mfma_f32_16x16x32_f16 v[70:73], v[142:145], v[174:177], v[70:73]
	v_mfma_f32_16x16x32_f16 v[66:69], v[150:153], v[174:177], v[66:69]
	s_waitcnt lgkmcnt(0)
	v_mfma_f32_16x16x32_f16 v[58:61], v[142:145], v[182:185], v[58:61]
	v_mfma_f32_16x16x32_f16 v[54:57], v[150:153], v[182:185], v[54:57]
	s_barrier
	s_mov_b32 m0, s58
	ds_read_b128 v[130:133], v138 offset:4096
	ds_read_b128 v[142:145], v138 offset:5120
	global_load_lds_dwordx4 v112, s[80:81]
	s_add_i32 m0, s58, 0x2000
	s_nop 0
	global_load_lds_dwordx4 v116, s[80:81]
	s_add_i32 m0, s58, 0x4000
	s_nop 0
	global_load_lds_dwordx4 v118, s[80:81]
	s_cmp_lg_u32 s67, 0
	s_cbranch_scc1 .Lpj_norm_2
	global_load_dwordx4 v[34:37], v[198:199], off offset:128
	global_load_dwordx4 v[38:41], v[200:201], off
	global_load_dwordx4 v[42:45], v[200:201], off offset:64
	global_load_dwordx4 v[46:49], v[200:201], off offset:128
	s_waitcnt vmcnt(13)
	s_branch .Lpj_join_2

.Lpj_join_2:
	s_barrier
	s_waitcnt lgkmcnt(1)
	v_mfma_f32_16x16x32_f16 v[86:89], v[130:133], v[154:157], v[86:89]
	v_mfma_f32_16x16x32_f16 v[74:77], v[130:133], v[162:165], v[74:77]
	v_mfma_f32_16x16x32_f16 v[62:65], v[130:133], v[170:173], v[62:65]
	v_mfma_f32_16x16x32_f16 v[50:53], v[130:133], v[178:181], v[50:53]
	s_waitcnt lgkmcnt(0)
	v_mfma_f32_16x16x32_f16 v[86:89], v[142:145], v[158:161], v[86:89]
	v_mfma_f32_16x16x32_f16 v[74:77], v[142:145], v[166:169], v[74:77]
	v_mfma_f32_16x16x32_f16 v[62:65], v[142:145], v[174:177], v[62:65]
	v_mfma_f32_16x16x32_f16 v[50:53], v[142:145], v[182:185], v[50:53]
	s_add_i32 s67, s67, 3
	s_add_u32 s30, s30, 0x180
	s_addc_u32 s31, s31, 0
	s_cmp_ge_i32 s67, s59
	s_cbranch_scc1 .Lrot_exit_proj
	s_add_u32 s74, s26, s30
	s_addc_u32 s75, s27, s31
	s_add_u32 s76, s28, s30
	s_addc_u32 s77, s29, s31
	s_add_u32 s34, s26, s30
	s_addc_u32 s35, s27, s31
	s_add_u32 s34, s34, 0x180
	s_addc_u32 s35, s35, 0
	s_add_u32 s68, s28, s30
	s_addc_u32 s69, s29, s31
	s_add_u32 s70, s68, 0x180
	s_addc_u32 s71, s69, 0
	s_cmp_eq_u32 s60, s67
	s_cselect_b32 s69, s5, s35
	s_cselect_b32 s68, s4, s34
	s_cselect_b32 s35, s7, s71
	s_cselect_b32 s34, s6, s70
	s_add_u32 s78, s68, 0x80
	s_addc_u32 s79, s69, 0
	s_add_u32 s80, s34, 0x80
	s_addc_u32 s81, s35, 0
	s_add_i32 s70, s62, s44
	s_barrier
	s_branch .LBB4_22

.LBB5_55:
	s_mov_b32 m0, s76
	ds_read_b128 v[44:47], v130 offset:16384
	ds_read_b128 v[56:59], v130 offset:17408
	ds_read_b128 v[60:63], v130 offset:18432
	ds_read_b128 v[64:67], v130 offset:19456
	ds_read_b128 v[68:71], v131
	ds_read_b128 v[96:99], v131 offset:1024
	ds_read_b128 v[136:139], v131 offset:2048
	ds_read_b128 v[140:143], v131 offset:3072
	ds_read_b128 v[144:147], v131 offset:4096
	ds_read_b128 v[148:151], v131 offset:5120
	ds_read_b128 v[152:155], v131 offset:6144
	ds_read_b128 v[156:159], v131 offset:7168
	global_load_lds_dwordx4 v112, s[78:79]
	s_add_i32 m0, s76, 0x2000
	s_add_i32 s76, s27, s54
	global_load_lds_dwordx4 v114, s[78:79]
	s_mov_b32 m0, s76
	s_nop 0
	global_load_lds_dwordx4 v116, s[80:81]
	s_add_i32 m0, s76, 0x2000
	s_nop 0
	global_load_lds_dwordx4 v118, s[80:81]
	s_barrier
	s_waitcnt lgkmcnt(7)
	v_mfma_f32_16x16x32_f16 v[92:95], v[44:47], v[68:71], v[92:95]
	v_mfma_f32_16x16x32_f16 v[88:91], v[60:63], v[68:71], v[88:91]
	s_waitcnt lgkmcnt(5)
	v_mfma_f32_16x16x32_f16 v[76:79], v[44:47], v[136:139], v[76:79]
	v_mfma_f32_16x16x32_f16 v[72:75], v[60:63], v[136:139], v[72:75]
	s_waitcnt lgkmcnt(3)
	v_mfma_f32_16x16x32_f16 v[28:31], v[44:47], v[144:147], v[28:31]
	v_mfma_f32_16x16x32_f16 v[24:27], v[60:63], v[144:147], v[24:27]
	s_waitcnt lgkmcnt(1)
	v_mfma_f32_16x16x32_f16 v[12:15], v[44:47], v[152:155], v[12:15]
	v_mfma_f32_16x16x32_f16 v[8:11], v[60:63], v[152:155], v[8:11]
	v_mfma_f32_16x16x32_f16 v[92:95], v[56:59], v[96:99], v[92:95]
	v_mfma_f32_16x16x32_f16 v[88:91], v[64:67], v[96:99], v[88:91]
	v_mfma_f32_16x16x32_f16 v[76:79], v[56:59], v[140:143], v[76:79]
	v_mfma_f32_16x16x32_f16 v[72:75], v[64:67], v[140:143], v[72:75]
	v_mfma_f32_16x16x32_f16 v[28:31], v[56:59], v[148:151], v[28:31]
	v_mfma_f32_16x16x32_f16 v[24:27], v[64:67], v[148:151], v[24:27]
	s_waitcnt lgkmcnt(0)
	v_mfma_f32_16x16x32_f16 v[12:15], v[56:59], v[156:159], v[12:15]
	v_mfma_f32_16x16x32_f16 v[8:11], v[64:67], v[156:159], v[8:11]
	s_barrier
	s_add_i32 s76, s68, s54
	s_mov_b32 m0, s76
	ds_read_b128 v[44:47], v130 offset:32768
	ds_read_b128 v[56:59], v130 offset:33792
	ds_read_b128 v[60:63], v130 offset:34816
	ds_read_b128 v[64:67], v130 offset:35840
	global_load_lds_dwordx4 v120, s[80:81]
	s_add_i32 m0, s76, 0x2000
	s_nop 0
	global_load_lds_dwordx4 v122, s[80:81]
	s_waitcnt vmcnt(6)
	s_barrier
	s_waitcnt lgkmcnt(3)
	v_mfma_f32_16x16x32_f16 v[84:87], v[44:47], v[68:71], v[84:87]
	v_mfma_f32_16x16x32_f16 v[52:55], v[44:47], v[136:139], v[52:55]
	s_waitcnt lgkmcnt(1)
	v_mfma_f32_16x16x32_f16 v[48:51], v[60:63], v[136:139], v[48:51]
	v_mfma_f32_16x16x32_f16 v[20:23], v[44:47], v[144:147], v[20:23]
	v_mfma_f32_16x16x32_f16 v[16:19], v[60:63], v[144:147], v[16:19]
	v_mfma_f32_16x16x32_f16 v[4:7], v[44:47], v[152:155], v[4:7]
	v_mfma_f32_16x16x32_f16 v[0:3], v[60:63], v[152:155], v[0:3]
	v_mfma_f32_16x16x32_f16 v[84:87], v[56:59], v[96:99], v[84:87]
	v_mfma_f32_16x16x32_f16 v[68:71], v[60:63], v[68:71], v[80:83]
	v_mfma_f32_16x16x32_f16 v[52:55], v[56:59], v[140:143], v[52:55]
	s_waitcnt lgkmcnt(0)
	v_mfma_f32_16x16x32_f16 v[48:51], v[64:67], v[140:143], v[48:51]
	v_mfma_f32_16x16x32_f16 v[20:23], v[56:59], v[148:151], v[20:23]
	v_mfma_f32_16x16x32_f16 v[16:19], v[64:67], v[148:151], v[16:19]
	v_mfma_f32_16x16x32_f16 v[4:7], v[56:59], v[156:159], v[4:7]
	v_mfma_f32_16x16x32_f16 v[0:3], v[64:67], v[156:159], v[0:3]
	v_mfma_f32_16x16x32_f16 v[68:71], v[64:67], v[96:99], v[68:71]
	s_barrier
	s_add_i32 s76, 0, 0x10000
	s_mov_b32 m0, s57
	v_add_u32_e32 v64, s76, v128
	ds_read_b128 v[44:47], v64
	ds_read_b128 v[56:59], v64 offset:1024
	ds_read_b128 v[60:63], v64 offset:2048
	ds_read_b128 v[64:67], v64 offset:3072
	ds_read_b128 v[80:83], v131 offset:49152
	ds_read_b128 v[96:99], v131 offset:50176
	ds_read_b128 v[136:139], v131 offset:51200
	ds_read_b128 v[140:143], v131 offset:52224
	ds_read_b128 v[144:147], v131 offset:53248
	ds_read_b128 v[148:151], v131 offset:54272
	ds_read_b128 v[152:155], v131 offset:55296
	ds_read_b128 v[156:159], v131 offset:56320
	global_load_lds_dwordx4 v100, s[48:49]
	s_mov_b32 m0, s58
	s_nop 0
	global_load_lds_dwordx4 v104, s[48:49]
	s_mov_b32 m0, s59
	s_nop 0
	global_load_lds_dwordx4 v102, s[46:47]
	s_mov_b32 m0, s60
	s_nop 0
	global_load_lds_dwordx4 v106, s[46:47]
	s_barrier
	s_waitcnt lgkmcnt(7)
	v_mfma_f32_16x16x32_f16 v[92:95], v[44:47], v[80:83], v[92:95]
	v_mfma_f32_16x16x32_f16 v[88:91], v[60:63], v[80:83], v[88:91]
	s_waitcnt lgkmcnt(5)
	v_mfma_f32_16x16x32_f16 v[76:79], v[44:47], v[136:139], v[76:79]
	v_mfma_f32_16x16x32_f16 v[72:75], v[60:63], v[136:139], v[72:75]
	s_waitcnt lgkmcnt(3)
	v_mfma_f32_16x16x32_f16 v[28:31], v[44:47], v[144:147], v[28:31]
	v_mfma_f32_16x16x32_f16 v[24:27], v[60:63], v[144:147], v[24:27]
	s_waitcnt lgkmcnt(1)
	v_mfma_f32_16x16x32_f16 v[12:15], v[44:47], v[152:155], v[12:15]
	v_mfma_f32_16x16x32_f16 v[8:11], v[60:63], v[152:155], v[8:11]
	v_mfma_f32_16x16x32_f16 v[92:95], v[56:59], v[96:99], v[92:95]
	v_mfma_f32_16x16x32_f16 v[88:91], v[64:67], v[96:99], v[88:91]
	v_mfma_f32_16x16x32_f16 v[76:79], v[56:59], v[140:143], v[76:79]
	v_mfma_f32_16x16x32_f16 v[72:75], v[64:67], v[140:143], v[72:75]
	v_mfma_f32_16x16x32_f16 v[28:31], v[56:59], v[148:151], v[28:31]
	v_mfma_f32_16x16x32_f16 v[24:27], v[64:67], v[148:151], v[24:27]
	s_waitcnt lgkmcnt(0)
	v_mfma_f32_16x16x32_f16 v[12:15], v[56:59], v[156:159], v[12:15]
	v_mfma_f32_16x16x32_f16 v[8:11], v[64:67], v[156:159], v[8:11]
	s_barrier
	s_add_i32 s48, 0, 0x14000
	s_add_u32 s46, s46, s10
	s_addc_u32 s47, s47, s11
	s_mov_b32 m0, s61
	v_add_u32_e32 v64, s48, v128
	ds_read_b128 v[44:47], v64
	ds_read_b128 v[56:59], v64 offset:1024
	ds_read_b128 v[60:63], v64 offset:2048
	ds_read_b128 v[64:67], v64 offset:3072
	global_load_lds_dwordx4 v102, s[46:47]
	s_mov_b32 m0, s62
	s_nop 0
	global_load_lds_dwordx4 v106, s[46:47]
	s_waitcnt vmcnt(6)
	s_barrier
	s_waitcnt lgkmcnt(3)
	v_mfma_f32_16x16x32_f16 v[84:87], v[44:47], v[80:83], v[84:87]
	v_mfma_f32_16x16x32_f16 v[52:55], v[44:47], v[136:139], v[52:55]
	s_waitcnt lgkmcnt(1)
	v_mfma_f32_16x16x32_f16 v[48:51], v[60:63], v[136:139], v[48:51]
	v_mfma_f32_16x16x32_f16 v[20:23], v[44:47], v[144:147], v[20:23]
	v_mfma_f32_16x16x32_f16 v[16:19], v[60:63], v[144:147], v[16:19]
	v_mfma_f32_16x16x32_f16 v[4:7], v[44:47], v[152:155], v[4:7]
	v_mfma_f32_16x16x32_f16 v[0:3], v[60:63], v[152:155], v[0:3]
	v_mfma_f32_16x16x32_f16 v[84:87], v[56:59], v[96:99], v[84:87]
	v_mfma_f32_16x16x32_f16 v[68:71], v[60:63], v[80:83], v[68:71]
	v_mfma_f32_16x16x32_f16 v[52:55], v[56:59], v[140:143], v[52:55]
	s_waitcnt lgkmcnt(0)
	v_mfma_f32_16x16x32_f16 v[48:51], v[64:67], v[140:143], v[48:51]
	v_mfma_f32_16x16x32_f16 v[20:23], v[56:59], v[148:151], v[20:23]
	v_mfma_f32_16x16x32_f16 v[16:19], v[64:67], v[148:151], v[16:19]
	v_mfma_f32_16x16x32_f16 v[4:7], v[56:59], v[156:159], v[4:7]
	v_mfma_f32_16x16x32_f16 v[0:3], v[64:67], v[156:159], v[0:3]
	v_mfma_f32_16x16x32_f16 v[68:71], v[64:67], v[96:99], v[68:71]
	s_barrier
	s_mov_b32 m0, s64
	ds_read_b128 v[44:47], v132
	ds_read_b128 v[56:59], v132 offset:1024
	ds_read_b128 v[60:63], v132 offset:2048
	ds_read_b128 v[64:67], v132 offset:3072
	ds_read_b128 v[80:83], v133
	ds_read_b128 v[96:99], v133 offset:1024
	ds_read_b128 v[136:139], v133 offset:2048
	ds_read_b128 v[140:143], v133 offset:3072
	ds_read_b128 v[144:147], v133 offset:4096
	ds_read_b128 v[148:151], v133 offset:5120
	ds_read_b128 v[152:155], v133 offset:6144
	ds_read_b128 v[156:159], v133 offset:7168
	global_load_lds_dwordx4 v100, s[82:83]
	s_mov_b32 m0, s65
	s_add_i32 s46, s76, s54
	global_load_lds_dwordx4 v104, s[82:83]
	s_mov_b32 m0, s46
	s_nop 0
	global_load_lds_dwordx4 v102, s[84:85]
	s_add_i32 m0, s46, 0x2000
	s_nop 0
	global_load_lds_dwordx4 v106, s[84:85]
	s_barrier
	s_waitcnt lgkmcnt(7)
	v_mfma_f32_16x16x32_f16 v[92:95], v[44:47], v[80:83], v[92:95]
	v_mfma_f32_16x16x32_f16 v[88:91], v[60:63], v[80:83], v[88:91]
	s_waitcnt lgkmcnt(5)
	v_mfma_f32_16x16x32_f16 v[76:79], v[44:47], v[136:139], v[76:79]
	v_mfma_f32_16x16x32_f16 v[72:75], v[60:63], v[136:139], v[72:75]
	s_waitcnt lgkmcnt(3)
	v_mfma_f32_16x16x32_f16 v[28:31], v[44:47], v[144:147], v[28:31]
	v_mfma_f32_16x16x32_f16 v[24:27], v[60:63], v[144:147], v[24:27]
	s_waitcnt lgkmcnt(1)
	v_mfma_f32_16x16x32_f16 v[12:15], v[44:47], v[152:155], v[12:15]
	v_mfma_f32_16x16x32_f16 v[8:11], v[60:63], v[152:155], v[8:11]
	v_mfma_f32_16x16x32_f16 v[92:95], v[56:59], v[96:99], v[92:95]
	v_mfma_f32_16x16x32_f16 v[88:91], v[64:67], v[96:99], v[88:91]
	v_mfma_f32_16x16x32_f16 v[76:79], v[56:59], v[140:143], v[76:79]
	v_mfma_f32_16x16x32_f16 v[72:75], v[64:67], v[140:143], v[72:75]
	v_mfma_f32_16x16x32_f16 v[28:31], v[56:59], v[148:151], v[28:31]
	v_mfma_f32_16x16x32_f16 v[24:27], v[64:67], v[148:151], v[24:27]
	s_waitcnt lgkmcnt(0)
	v_mfma_f32_16x16x32_f16 v[12:15], v[56:59], v[156:159], v[12:15]
	v_mfma_f32_16x16x32_f16 v[8:11], v[64:67], v[156:159], v[8:11]
	s_barrier
	s_add_i32 s46, s48, s54
	s_mov_b32 m0, s46
	ds_read_b128 v[44:47], v134
	ds_read_b128 v[56:59], v134 offset:1024
	ds_read_b128 v[60:63], v134 offset:2048
	ds_read_b128 v[64:67], v134 offset:3072
	global_load_lds_dwordx4 v102, s[86:87]
	s_add_i32 m0, s46, 0x2000
	s_nop 0
	global_load_lds_dwordx4 v106, s[86:87]
	s_waitcnt vmcnt(6)
	s_barrier
	s_waitcnt lgkmcnt(3)
	v_mfma_f32_16x16x32_f16 v[84:87], v[44:47], v[80:83], v[84:87]
	s_waitcnt lgkmcnt(1)
	v_mfma_f32_16x16x32_f16 v[68:71], v[60:63], v[80:83], v[68:71]
	v_mfma_f32_16x16x32_f16 v[52:55], v[44:47], v[136:139], v[52:55]
	v_mfma_f32_16x16x32_f16 v[48:51], v[60:63], v[136:139], v[48:51]
	v_mfma_f32_16x16x32_f16 v[20:23], v[44:47], v[144:147], v[20:23]
	v_mfma_f32_16x16x32_f16 v[16:19], v[60:63], v[144:147], v[16:19]
	v_mfma_f32_16x16x32_f16 v[4:7], v[44:47], v[152:155], v[4:7]
	v_mfma_f32_16x16x32_f16 v[0:3], v[60:63], v[152:155], v[0:3]
	v_mfma_f32_16x16x32_f16 v[84:87], v[56:59], v[96:99], v[84:87]
	s_waitcnt lgkmcnt(0)
	v_mfma_f32_16x16x32_f16 v[80:83], v[64:67], v[96:99], v[68:71]
	v_mfma_f32_16x16x32_f16 v[52:55], v[56:59], v[140:143], v[52:55]
	v_mfma_f32_16x16x32_f16 v[48:51], v[64:67], v[140:143], v[48:51]
	v_mfma_f32_16x16x32_f16 v[20:23], v[56:59], v[148:151], v[20:23]
	v_mfma_f32_16x16x32_f16 v[16:19], v[64:67], v[148:151], v[16:19]
	v_mfma_f32_16x16x32_f16 v[4:7], v[56:59], v[156:159], v[4:7]
	v_mfma_f32_16x16x32_f16 v[0:3], v[64:67], v[156:159], v[0:3]
	s_add_i32 s75, s75, 3
	s_add_u32 s44, s44, 0x180
	s_addc_u32 s45, s45, 0
	s_cmp_ge_i32 s75, s66
	s_cbranch_scc1 .Lrot_exit_mlp1
	s_add_u32 s78, s40, s44
	s_addc_u32 s79, s41, s45
	s_add_u32 s80, s42, s44
	s_addc_u32 s81, s43, s45
	s_add_u32 s46, s40, s44
	s_addc_u32 s47, s41, s45
	s_add_u32 s46, s46, 0x180
	s_addc_u32 s47, s47, 0
	s_add_u32 s48, s42, s44
	s_addc_u32 s49, s43, s45
	s_add_u32 s76, s48, 0x180
	s_addc_u32 s77, s49, 0
	s_cmp_eq_u32 s67, s75
	s_cselect_b32 s49, s7, s47
	s_cselect_b32 s48, s6, s46
	s_cselect_b32 s47, s5, s77
	s_cselect_b32 s46, s4, s76
	s_add_u32 s82, s48, 0x80
	s_addc_u32 s83, s49, 0
	s_add_u32 s84, s46, 0x80
	s_addc_u32 s85, s47, 0
	s_add_u32 s86, s84, s10
	s_addc_u32 s87, s85, s11
	s_add_i32 s76, s19, s54
	s_barrier
	s_branch .LBB5_55

.LBB6_22:
	s_mov_b32 m0, s68
	ds_read_b128 v[132:135], v131 offset:16384
	ds_read_b128 v[136:139], v131 offset:17408
	ds_read_b128 v[140:143], v131 offset:18432
	ds_read_b128 v[144:147], v131 offset:19456
	ds_read_b128 v[148:151], v182
	ds_read_b128 v[152:155], v182 offset:1024
	ds_read_b128 v[156:159], v182 offset:2048
	ds_read_b128 v[160:163], v182 offset:3072
	ds_read_b128 v[164:167], v182 offset:4096
	ds_read_b128 v[168:171], v182 offset:5120
	ds_read_b128 v[172:175], v182 offset:6144
	ds_read_b128 v[176:179], v182 offset:7168
	global_load_lds_dwordx4 v106, s[72:73]
	s_add_i32 m0, s68, 0x2000
	s_nop 0
	global_load_lds_dwordx4 v108, s[72:73]
	s_barrier
	s_waitcnt lgkmcnt(7)
	v_mfma_f32_16x16x32_f16 v[40:43], v[132:135], v[148:151], v[40:43]
	v_mfma_f32_16x16x32_f16 v[44:47], v[140:143], v[148:151], v[44:47]
	s_waitcnt lgkmcnt(5)
	v_mfma_f32_16x16x32_f16 v[32:35], v[132:135], v[156:159], v[32:35]
	v_mfma_f32_16x16x32_f16 v[28:31], v[140:143], v[156:159], v[28:31]
	s_waitcnt lgkmcnt(3)
	v_mfma_f32_16x16x32_f16 v[20:23], v[132:135], v[164:167], v[20:23]
	v_mfma_f32_16x16x32_f16 v[16:19], v[140:143], v[164:167], v[16:19]
	s_waitcnt lgkmcnt(1)
	v_mfma_f32_16x16x32_f16 v[8:11], v[132:135], v[172:175], v[8:11]
	v_mfma_f32_16x16x32_f16 v[4:7], v[140:143], v[172:175], v[4:7]
	v_mfma_f32_16x16x32_f16 v[40:43], v[136:139], v[152:155], v[40:43]
	v_mfma_f32_16x16x32_f16 v[44:47], v[144:147], v[152:155], v[44:47]
	v_mfma_f32_16x16x32_f16 v[32:35], v[136:139], v[160:163], v[32:35]
	v_mfma_f32_16x16x32_f16 v[28:31], v[144:147], v[160:163], v[28:31]
	v_mfma_f32_16x16x32_f16 v[20:23], v[136:139], v[168:171], v[20:23]
	v_mfma_f32_16x16x32_f16 v[16:19], v[144:147], v[168:171], v[16:19]
	s_waitcnt lgkmcnt(0)
	v_mfma_f32_16x16x32_f16 v[8:11], v[136:139], v[176:179], v[8:11]
	v_mfma_f32_16x16x32_f16 v[4:7], v[144:147], v[176:179], v[4:7]
	s_barrier
	s_add_i32 m0, s47, 0x18000
	ds_read_b128 v[132:135], v131 offset:20480
	ds_read_b128 v[136:139], v131 offset:21504
	global_load_lds_dwordx4 v110, s[74:75]
	s_add_i32 m0, s47, 0x1a000
	s_nop 0
	global_load_lds_dwordx4 v112, s[74:75]
	s_add_i32 m0, s47, 0x1c000
	s_nop 0
	global_load_lds_dwordx4 v114, s[74:75]
	s_cmp_lg_u32 s65, 0
	s_cbranch_scc1 .Lm2_norm_0
	s_mul_i32 s70, s58, 0xc0
	v_add_u32_e32 v234, s70, v129
	v_ashrrev_i32_e32 v235, 31, v234
	v_lshlrev_b64 v[234:235], 2, v[234:235]
	v_lshl_add_u64 v[234:235], s[18:19], 0, v[234:235]
	global_load_dwordx4 v[222:225], v[234:235], off
	global_load_dwordx4 v[226:229], v[234:235], off offset:64
	global_load_dwordx4 v[230:233], v[234:235], off offset:128
	global_load_dwordx2 v[198:199], v[190:191], off
	global_load_dwordx2 v[200:201], v[190:191], off offset:32
	global_load_dwordx2 v[202:203], v[190:191], off offset:64
	global_load_dwordx2 v[204:205], v[192:193], off
	s_waitcnt vmcnt(12)
	s_branch .Lm2_join_0

.Lm2_join_0:
	s_barrier
	s_waitcnt lgkmcnt(1)
	v_mfma_f32_16x16x32_f16 v[36:39], v[132:135], v[148:151], v[36:39]
	v_mfma_f32_16x16x32_f16 v[24:27], v[132:135], v[156:159], v[24:27]
	v_mfma_f32_16x16x32_f16 v[12:15], v[132:135], v[164:167], v[12:15]
	v_mfma_f32_16x16x32_f16 v[0:3], v[132:135], v[172:175], v[0:3]
	s_waitcnt lgkmcnt(0)
	v_mfma_f32_16x16x32_f16 v[36:39], v[136:139], v[152:155], v[36:39]
	v_mfma_f32_16x16x32_f16 v[24:27], v[136:139], v[160:163], v[24:27]
	v_mfma_f32_16x16x32_f16 v[12:15], v[136:139], v[168:171], v[12:15]
	v_mfma_f32_16x16x32_f16 v[0:3], v[136:139], v[176:179], v[0:3]
	s_barrier
	s_mov_b32 m0, s47
	ds_read_b128 v[132:135], v131 offset:57344
	ds_read_b128 v[136:139], v131 offset:58368
	ds_read_b128 v[140:143], v131 offset:59392
	ds_read_b128 v[144:147], v131 offset:60416
	ds_read_b128 v[148:151], v182 offset:40960
	ds_read_b128 v[152:155], v182 offset:41984
	ds_read_b128 v[156:159], v182 offset:43008
	ds_read_b128 v[160:163], v182 offset:44032
	ds_read_b128 v[164:167], v182 offset:45056
	ds_read_b128 v[168:171], v182 offset:46080
	ds_read_b128 v[172:175], v182 offset:47104
	ds_read_b128 v[176:179], v182 offset:48128
	global_load_lds_dwordx4 v48, s[66:67]
	s_mov_b32 m0, s48
	s_nop 0
	global_load_lds_dwordx4 v52, s[66:67]
	s_barrier
	s_waitcnt lgkmcnt(7)
	v_mfma_f32_16x16x32_f16 v[40:43], v[132:135], v[148:151], v[40:43]
	v_mfma_f32_16x16x32_f16 v[44:47], v[140:143], v[148:151], v[44:47]
	s_waitcnt lgkmcnt(5)
	v_mfma_f32_16x16x32_f16 v[32:35], v[132:135], v[156:159], v[32:35]
	v_mfma_f32_16x16x32_f16 v[28:31], v[140:143], v[156:159], v[28:31]
	s_waitcnt lgkmcnt(3)
	v_mfma_f32_16x16x32_f16 v[20:23], v[132:135], v[164:167], v[20:23]
	v_mfma_f32_16x16x32_f16 v[16:19], v[140:143], v[164:167], v[16:19]
	s_waitcnt lgkmcnt(1)
	v_mfma_f32_16x16x32_f16 v[8:11], v[132:135], v[172:175], v[8:11]
	v_mfma_f32_16x16x32_f16 v[4:7], v[140:143], v[172:175], v[4:7]
	v_mfma_f32_16x16x32_f16 v[40:43], v[136:139], v[152:155], v[40:43]
	v_mfma_f32_16x16x32_f16 v[44:47], v[144:147], v[152:155], v[44:47]
	v_mfma_f32_16x16x32_f16 v[32:35], v[136:139], v[160:163], v[32:35]
	v_mfma_f32_16x16x32_f16 v[28:31], v[144:147], v[160:163], v[28:31]
	v_mfma_f32_16x16x32_f16 v[20:23], v[136:139], v[168:171], v[20:23]
	v_mfma_f32_16x16x32_f16 v[16:19], v[144:147], v[168:171], v[16:19]
	s_waitcnt lgkmcnt(0)
	v_mfma_f32_16x16x32_f16 v[8:11], v[136:139], v[176:179], v[8:11]
	v_mfma_f32_16x16x32_f16 v[4:7], v[144:147], v[176:179], v[4:7]
	s_barrier
	s_mov_b32 m0, s49
	ds_read_b128 v[132:135], v131 offset:61440
	ds_read_b128 v[136:139], v131 offset:62464
	global_load_lds_dwordx4 v50, s[30:31]
	s_mov_b32 m0, s50
	s_nop 0
	global_load_lds_dwordx4 v54, s[30:31]
	s_mov_b32 m0, s51
	s_nop 0
	global_load_lds_dwordx4 v56, s[30:31]
	s_cmp_lg_u32 s65, 0
	s_cbranch_scc1 .Lm2_norm_1
	global_load_dwordx2 v[206:207], v[192:193], off offset:32
	global_load_dwordx2 v[208:209], v[192:193], off offset:64
	global_load_dwordx2 v[210:211], v[194:195], off
	global_load_dwordx2 v[212:213], v[194:195], off offset:32
	s_waitcnt vmcnt(16)
	s_branch .Lm2_join_1

.Lm2_join_1:
	s_barrier
	s_waitcnt lgkmcnt(1)
	v_mfma_f32_16x16x32_f16 v[36:39], v[132:135], v[148:151], v[36:39]
	v_mfma_f32_16x16x32_f16 v[24:27], v[132:135], v[156:159], v[24:27]
	v_mfma_f32_16x16x32_f16 v[12:15], v[132:135], v[164:167], v[12:15]
	v_mfma_f32_16x16x32_f16 v[0:3], v[132:135], v[172:175], v[0:3]
	s_waitcnt lgkmcnt(0)
	v_mfma_f32_16x16x32_f16 v[36:39], v[136:139], v[152:155], v[36:39]
	v_mfma_f32_16x16x32_f16 v[24:27], v[136:139], v[160:163], v[24:27]
	v_mfma_f32_16x16x32_f16 v[12:15], v[136:139], v[168:171], v[12:15]
	v_mfma_f32_16x16x32_f16 v[0:3], v[136:139], v[176:179], v[0:3]
	s_barrier
	s_mov_b32 m0, s54
	v_add_u32_e32 v131, s62, v127
	ds_read_b128 v[132:135], v130
	ds_read_b128 v[136:139], v130 offset:1024
	ds_read_b128 v[140:143], v130 offset:2048
	ds_read_b128 v[144:147], v130 offset:3072
	ds_read_b128 v[148:151], v131
	ds_read_b128 v[152:155], v131 offset:1024
	ds_read_b128 v[156:159], v131 offset:2048
	ds_read_b128 v[160:163], v131 offset:3072
	ds_read_b128 v[164:167], v131 offset:4096
	ds_read_b128 v[168:171], v131 offset:5120
	ds_read_b128 v[172:175], v131 offset:6144
	ds_read_b128 v[176:179], v131 offset:7168
	global_load_lds_dwordx4 v48, s[76:77]
	s_mov_b32 m0, s55
	s_nop 0
	global_load_lds_dwordx4 v52, s[76:77]
	s_barrier
	s_waitcnt lgkmcnt(7)
	v_mfma_f32_16x16x32_f16 v[40:43], v[132:135], v[148:151], v[40:43]
	v_mfma_f32_16x16x32_f16 v[44:47], v[140:143], v[148:151], v[44:47]
	s_waitcnt lgkmcnt(5)
	v_mfma_f32_16x16x32_f16 v[32:35], v[132:135], v[156:159], v[32:35]
	v_mfma_f32_16x16x32_f16 v[28:31], v[140:143], v[156:159], v[28:31]
	s_waitcnt lgkmcnt(3)
	v_mfma_f32_16x16x32_f16 v[20:23], v[132:135], v[164:167], v[20:23]
	v_mfma_f32_16x16x32_f16 v[16:19], v[140:143], v[164:167], v[16:19]
	s_waitcnt lgkmcnt(1)
	v_mfma_f32_16x16x32_f16 v[8:11], v[132:135], v[172:175], v[8:11]
	v_mfma_f32_16x16x32_f16 v[4:7], v[140:143], v[172:175], v[4:7]
	v_mfma_f32_16x16x32_f16 v[40:43], v[136:139], v[152:155], v[40:43]
	v_mfma_f32_16x16x32_f16 v[44:47], v[144:147], v[152:155], v[44:47]
	v_mfma_f32_16x16x32_f16 v[32:35], v[136:139], v[160:163], v[32:35]
	v_mfma_f32_16x16x32_f16 v[28:31], v[144:147], v[160:163], v[28:31]
	v_mfma_f32_16x16x32_f16 v[20:23], v[136:139], v[168:171], v[20:23]
	v_mfma_f32_16x16x32_f16 v[16:19], v[144:147], v[168:171], v[16:19]
	s_waitcnt lgkmcnt(0)
	v_mfma_f32_16x16x32_f16 v[8:11], v[136:139], v[176:179], v[8:11]
	v_mfma_f32_16x16x32_f16 v[4:7], v[144:147], v[176:179], v[4:7]
	s_barrier
	s_mov_b32 m0, s56
	ds_read_b128 v[132:135], v130 offset:4096
	ds_read_b128 v[136:139], v130 offset:5120
	global_load_lds_dwordx4 v50, s[78:79]
	s_add_i32 m0, s56, 0x2000
	s_nop 0
	global_load_lds_dwordx4 v54, s[78:79]
	s_add_i32 m0, s56, 0x4000
	s_nop 0
	global_load_lds_dwordx4 v56, s[78:79]
	s_cmp_lg_u32 s65, 0
	s_cbranch_scc1 .Lm2_norm_2
	global_load_dwordx2 v[214:215], v[194:195], off offset:64
	global_load_dwordx2 v[216:217], v[196:197], off
	global_load_dwordx2 v[218:219], v[196:197], off offset:32
	global_load_dwordx2 v[220:221], v[196:197], off offset:64
	s_waitcnt vmcnt(13)
	s_branch .Lm2_join_2

.Lm2_join_2:
	s_barrier
	s_waitcnt lgkmcnt(1)
	v_mfma_f32_16x16x32_f16 v[36:39], v[132:135], v[148:151], v[36:39]
	v_mfma_f32_16x16x32_f16 v[24:27], v[132:135], v[156:159], v[24:27]
	v_mfma_f32_16x16x32_f16 v[12:15], v[132:135], v[164:167], v[12:15]
	v_mfma_f32_16x16x32_f16 v[0:3], v[132:135], v[172:175], v[0:3]
	s_waitcnt lgkmcnt(0)
	v_mfma_f32_16x16x32_f16 v[36:39], v[136:139], v[152:155], v[36:39]
	v_mfma_f32_16x16x32_f16 v[24:27], v[136:139], v[160:163], v[24:27]
	v_mfma_f32_16x16x32_f16 v[12:15], v[136:139], v[168:171], v[12:15]
	v_mfma_f32_16x16x32_f16 v[0:3], v[136:139], v[176:179], v[0:3]
	s_add_i32 s65, s65, 3
	s_add_u32 s28, s28, 0x180
	s_addc_u32 s29, s29, 0
	s_cmp_ge_i32 s65, s59
	s_cbranch_scc1 .Lrot_exit_mlp2
	s_add_u32 s72, s22, s28
	s_addc_u32 s73, s23, s29
	s_add_u32 s74, s24, s28
	s_addc_u32 s75, s25, s29
	s_add_u32 s30, s22, s28
	s_addc_u32 s31, s23, s29
	s_add_u32 s30, s30, 0x180
	s_addc_u32 s31, s31, 0
	s_add_u32 s66, s24, s28
	s_addc_u32 s67, s25, s29
	s_add_u32 s68, s66, 0x180
	s_addc_u32 s69, s67, 0
	s_cmp_eq_u32 s60, s65
	s_cselect_b32 s67, s27, s31
	s_cselect_b32 s66, s26, s30
	s_cselect_b32 s31, s5, s69
	s_cselect_b32 s30, s4, s68
	s_add_u32 s76, s66, 0x80
	s_addc_u32 s77, s67, 0
	s_add_u32 s78, s30, 0x80
	s_addc_u32 s79, s31, 0
	s_add_i32 s68, s62, s42
	v_add_u32_e32 v131, 0, v128
	v_add_u32_e32 v182, 0, v127
	s_barrier
	s_branch .LBB6_22
